# lever 4: one static s_setprio 1 for waves 4-7 at attention main-loop entry, reset at loop exit
# speedup vs baseline: 1.0108x; 1.0108x over previous
; __device__ __forceinline__ int lane_id_now() { unsigned z = 0u; asm volatile("" : "+v"(z)); return (int)__builtin_amdgcn_mbcnt_hi(~0u, __builtin_amdgcn_mbcnt_lo(~0u, z)); }
; #define LAS __attribute__((address_space(3)))
; #define ROPE2(W, CL, CH, SL, SH) { const float a0 = bflo(xa.W), a1 = bfhi(xa.W), b0 = bflo(xb.W), b1 = bfhi(xb.W); \
;           ya.W = cvtpk(a0 * CL - b0 * SL, a1 * CH - b1 * SH); yb.W = cvtpk(b0 * CL + a0 * SL, b1 * CH + a1 * SH); }
; __device__ __forceinline__ void attn_unit(LAS unsigned char* lds, int b, int h, int qb, const bf16* Q  , const bf16* KV  , const bf16* KPE  ,
;                                           const float* ROPE  , bf16* O  , const int wave_) {
;     int tid_ = wave_ * 64 + lane_id_now(); asm volatile("" : "+v"(tid_));
;     const int tid = tid_, wid = __builtin_amdgcn_readfirstlane(tid >> 6), lane = tid & 63, r32 = lane & 31, hi = lane >> 5;
;     const int NT = ((15 - qb) * 128 + 128) / KVBLK;
;     const int qlo = (wid < 4 ? qb * 128 + wid * 32 : (15 - qb) * 128 + (wid - 4) * 32), qm = qlo + r32 - 4 * hi;
;     const size_t tok0 = (size_t)b * SEQ;
;     bf16x8 qr[12];
;     { const size_t t = tok0 + qlo + r32; const bf16* qp = Q + t * 1536 + h * 192 + hi * 8;
; #pragma unroll
;       for (int d0 = 0; d0 < 12; ++d0) qr[d0] = *(const bf16x8*)(qp + d0 * 16);
;       const float* rp = ROPE + t * 64 + hi * 8;
; #pragma unroll
;       for (int e = 0; e < 2; ++e) {
;           const f32x4 c0 = *(const f32x4*)(rp + 16 * e), c1 = *(const f32x4*)(rp + 16 * e + 4), s0 = *(const f32x4*)(rp + 32 + 16 * e), s1 = *(const f32x4*)(rp + 32 + 16 * e + 4);
;           const v4u xa = *reinterpret_cast<v4u*>(&qr[8 + e]), xb = *reinterpret_cast<v4u*>(&qr[10 + e]); v4u ya, yb;
;     ...
;           ROPE2(x, c0[0], c0[1], s0[0], s0[1]); ROPE2(y, c0[2], c0[3], s0[2], s0[3]); ROPE2(z, c1[0], c1[1], s1[0], s1[1]); ROPE2(w, c1[2], c1[3], s1[2], s1[3]);
;     ...
;           qr[8 + e] = *reinterpret_cast<bf16x8*>(&ya); qr[10 + e] = *reinterpret_cast<bf16x8*>(&yb); } }
; __global__ void __launch_bounds__(NTHR, 2) fwd(Args args) {
;     ...
;         const int vcu = (NG % 8 == 0) ? (bx % 8) * (NG / 8) + bx / 8 : bx;
;         if (vcu < BATCH * H * 8) { const int L = vcu, bh = L >> 3, qb = L & 7;
;             mla::attn_unit(lds + RING_OFF, bh >> 3, bh & 7, qb, WSP(bf16, WS_Q), WSP(bf16, WS_KV), WSP(bf16, WS_KPE), WSP(float, WS_ROPE), WSP(bf16, WS_ATTO), wave); }
.LBB0_718:
	s_cmpk_lt_i32 s93, 0x100
	s_cselect_b64 s[0:1], -1, 0
	v_writelane_b32 v254, s0, 58
	s_cmpk_gt_i32 s93, 0xff
	s_nop 0
	v_writelane_b32 v254, s1, 59
	s_cbranch_scc1 .LBB0_862
	v_mov_b32_e32 v0, 0
	s_lshl_b32 s1, s93, 7
	v_mbcnt_lo_u32_b32 v0, -1, v0
	v_mbcnt_hi_u32_b32 v0, -1, v0
	v_add_u32_e32 v159, s94, v0
	s_and_b32 s1, s1, 0x380
	s_xor_b32 s6, s1, 0x780
	v_readfirstlane_b32 s5, v159
	s_ashr_i32 s2, s5, 6
	s_add_i32 s3, s6, 0x80
	s_ashr_i32 s0, s93, 6
	s_bfe_u32 s4, s93, 0x30003
	s_lshr_b32 s3, s3, 6
	s_lshl_b32 s7, s2, 5
	s_addk_i32 s6, 0xff80
	s_cmp_lt_i32 s2, 4
	s_cselect_b32 s33, s1, s6
	s_add_i32 s33, s33, s7
	s_ashr_i32 s1, s0, 31
	s_lshl_b64 s[6:7], s[0:1], 11
	s_ashr_i32 s8, s33, 31
	s_add_u32 s6, s6, s33
	v_mov_b32_e32 v145, 0
	v_and_b32_e32 v144, 31, v159
	s_addc_u32 s7, s7, s8
	v_lshl_add_u64 v[0:1], s[6:7], 0, v[144:145]
	s_movk_i32 s8, 0xc00
	v_mov_b64_e32 v[2:3], s[78:79]
	v_writelane_b32 v254, s89, 60
	s_mov_b32 s89, s87
	s_mov_b64 s[86:87], s[6:7]
	v_mad_u64_u32 v[2:3], s[6:7], v0, s8, v[2:3]
	v_mad_i32_i24 v3, v1, s8, v3
	v_lshlrev_b64 v[0:1], 8, v[0:1]
	v_lshl_add_u64 v[0:1], s[78:79], 0, v[0:1]
	v_and_b32_e32 v4, 32, v159
	v_mov_b32_e32 v5, v145
	v_lshl_add_u64 v[0:1], v[0:1], 0, v[4:5]
	s_mov_b64 s[6:7], 0xba28000
	v_lshl_add_u64 v[34:35], v[0:1], 0, s[6:7]
	s_mov_b32 s6, 0xba28000
	v_add_co_u32_e32 v0, vcc, s6, v0
	s_mov_b32 s71, 0
	v_bfe_u32 v158, v159, 5, 1
	v_addc_co_u32_e32 v1, vcc, 0, v1, vcc
	global_load_dwordx4 v[10:13], v[34:35], off offset:128
	global_load_dwordx4 v[14:17], v[0:1], off
	s_mul_i32 s70, s4, 0x180
	v_lshl_add_u64 v[0:1], v[2:3], 0, s[70:71]
	v_lshlrev_b32_e32 v8, 4, v158
	v_mov_b32_e32 v9, v145
	v_lshl_add_u64 v[4:5], v[0:1], 0, v[8:9]
	s_mov_b64 s[6:7], 0xbc28000
	v_lshl_add_u64 v[6:7], v[4:5], 0, s[6:7]
	global_load_dwordx4 v[18:21], v[6:7], off offset:256
	global_load_dwordx4 v[22:25], v[6:7], off offset:320
	global_load_dwordx4 v[26:29], v[34:35], off offset:144
	global_load_dwordx4 v[30:33], v[34:35], off offset:16
	global_load_dwordx4 v[96:99], v[6:7], off offset:224
	global_load_dwordx4 v[0:3], v[6:7], off offset:288
	s_mov_b32 s6, 0xbc28000
	v_add_co_u32_e32 v4, vcc, s6, v4
	s_and_b32 s5, s5, 0x3fffffc0
	s_nop 0
	v_addc_co_u32_e32 v5, vcc, 0, v5, vcc
	global_load_dwordx4 v[100:103], v[6:7], off offset:32
	global_load_dwordx4 v[104:107], v[6:7], off offset:64
	global_load_dwordx4 v[108:111], v[6:7], off offset:96
	global_load_dwordx4 v[112:115], v[6:7], off offset:128
	global_load_dwordx4 v[116:119], v[6:7], off offset:160
	global_load_dwordx4 v[120:123], v[6:7], off offset:192
	global_load_dwordx4 v[124:127], v[4:5], off
	s_nop 0
	global_load_dwordx4 v[4:7], v[6:7], off offset:352
	s_lshl_b32 s5, s5, 2
	s_add_i32 s5, s5, 0
	s_mov_b32 s74, s92
	s_add_i32 s6, s5, 0x1e000
	s_lshl_b32 s92, s4, 8
	s_lshl_b64 s[4:5], s[0:1], 23
	s_add_u32 s4, s78, s4
	v_writelane_b32 v254, s90, 61
	s_addc_u32 s5, s79, s5
	v_mov_b32_e32 v151, v145
	v_writelane_b32 v254, s91, 62
	s_mov_b64 s[90:91], s[84:85]
	s_mov_b32 s84, s96
	s_add_u32 s96, s4, 0xd428000
	s_mov_b32 s85, s97
	s_addc_u32 s97, s5, 0
	s_lshl_b64 s[0:1], s[0:1], 18
	s_add_u32 s0, s78, s0
	s_addc_u32 s1, s79, s1
	s_lshl_b32 s2, s2, 10
	s_mov_b64 s[66:67], 0x100
	s_add_i32 s95, s2, 0
	s_mov_b32 m0, s95
	v_mov_b32_e32 v153, v145
	v_mov_b32_e32 v147, v145
	v_mov_b32_e32 v149, v145
	v_lshlrev_b32_e32 v156, 2, v158
	v_add_u32_e32 v157, s6, v8
	s_mov_b32 s75, s88
	s_mov_b32 s88, s94
	s_mov_b32 s94, 63
	v_lshlrev_b32_e32 v160, 8, v144
	v_lshlrev_b32_e32 v166, 7, v144
	v_lshl_add_u32 v164, v144, 2, s6
	v_mov_b32_e32 v175, 0xf149f2ca
	s_mov_b32 s69, 0x14000
	v_mov_b32_e32 v173, 0xff800000
	s_mov_b32 s72, 0
	s_mov_b32 s73, 0
	s_waitcnt vmcnt(15)
	v_mov_b32_e32 v36, v10
	v_mov_b32_e32 v39, v10
	s_waitcnt vmcnt(14)
	v_mov_b32_e32 v10, v15
	v_mov_b32_e32 v37, v14
	s_waitcnt vmcnt(13)
	v_and_b32_e32 v47, 0xffff0000, v18
	s_waitcnt vmcnt(12)
	v_and_b32_e32 v46, 0xffff0000, v22
	v_mov_b32_e32 v38, v14
	v_mov_b32_e32 v14, v11
	v_lshlrev_b32_e32 v45, 16, v18
	v_lshlrev_b32_e32 v44, 16, v22
	v_pk_mul_f32 v[10:11], v[10:11], v[46:47]
	v_mov_b32_e32 v42, v16
	v_mov_b32_e32 v43, v12
	v_lshlrev_b32_e32 v49, 16, v19
	v_lshlrev_b32_e32 v48, 16, v23
	v_pk_mul_f32 v[36:37], v[36:37], v[44:45]
	v_pk_mul_f32 v[38:39], v[38:39], v[44:45]
	v_pk_mul_f32 v[14:15], v[14:15], v[46:47]
	v_add_f32_e32 v10, v10, v11
	v_mov_b32_e32 v40, v12
	v_sub_f32_e32 v9, v37, v36
	v_add_f32_e32 v12, v38, v39
	v_sub_f32_e32 v14, v15, v14
	v_cvt_pk_bf16_f32 v128, v9, v14
	v_cvt_pk_bf16_f32 v132, v12, v10
	v_pk_mul_f32 v[10:11], v[42:43], v[48:49]
	v_mov_b32_e32 v41, v16
	v_add_f32_e32 v9, v10, v11
	v_and_b32_e32 v11, 0xffff0000, v19
	v_and_b32_e32 v10, 0xffff0000, v23
	v_mov_b32_e32 v16, v13
	v_pk_mul_f32 v[14:15], v[16:17], v[10:11]
	v_pk_mul_f32 v[40:41], v[40:41], v[48:49]
	v_sub_f32_e32 v12, v15, v14
	v_sub_f32_e32 v18, v41, v40
	v_cvt_pk_bf16_f32 v129, v18, v12
	v_mov_b32_e32 v12, v17
	v_pk_mul_f32 v[10:11], v[12:13], v[10:11]
	s_waitcnt vmcnt(11)
	v_mov_b32_e32 v12, v26
	v_add_f32_e32 v10, v10, v11
	v_cvt_pk_bf16_f32 v133, v9, v10
	v_lshlrev_b32_e32 v11, 16, v20
	v_lshlrev_b32_e32 v10, 16, v24
	s_waitcnt vmcnt(10)
	v_mov_b32_e32 v13, v30
	v_pk_mul_f32 v[12:13], v[12:13], v[10:11]
	s_nop 0
	v_sub_f32_e32 v9, v13, v12
	v_mov_b32_e32 v12, v30
	v_mov_b32_e32 v13, v26
	v_pk_mul_f32 v[10:11], v[12:13], v[10:11]
	v_mov_b32_e32 v30, v27
	v_add_f32_e32 v14, v10, v11
	v_and_b32_e32 v11, 0xffff0000, v20
	v_and_b32_e32 v10, 0xffff0000, v24
	v_pk_mul_f32 v[12:13], v[30:31], v[10:11]
	v_mov_b32_e32 v26, v31
	v_sub_f32_e32 v12, v13, v12
	v_pk_mul_f32 v[10:11], v[26:27], v[10:11]
	v_cvt_pk_bf16_f32 v130, v9, v12
	v_mov_b32_e32 v12, v28
	v_add_f32_e32 v9, v10, v11
	v_lshlrev_b32_e32 v11, 16, v21
	v_lshlrev_b32_e32 v10, 16, v25
	v_mov_b32_e32 v13, v32
	v_pk_mul_f32 v[12:13], v[12:13], v[10:11]
	v_cvt_pk_bf16_f32 v134, v14, v9
	s_waitcnt vmcnt(8)
; #define LAS __attribute__((address_space(3)))
; __device__ __forceinline__ int v_rd_base(int lane) { return ((lane & 3) << 3) | (((lane >> 2) & 3) << 6) | (((lane >> 4) & 1) << 5) | (((lane >> 5) & 1) << 8); }
; #define ROPE2(W, CL, CH, SL, SH) { const float a0 = bflo(xa.W), a1 = bfhi(xa.W), b0 = bflo(xb.W), b1 = bfhi(xb.W); \
;           ya.W = cvtpk(a0 * CL - b0 * SL, a1 * CH - b1 * SH); yb.W = cvtpk(b0 * CL + a0 * SL, b1 * CH + a1 * SH); }
; __device__ __forceinline__ void attn_unit(LAS unsigned char* lds, int b, int h, int qb, const bf16* Q  , const bf16* KV  , const bf16* KPE  ,
;                                           const float* ROPE  , bf16* O  , const int wave_) {
;     ...
;       for (int e = 0; e < 2; ++e) {
;           const f32x4 c0 = *(const f32x4*)(rp + 16 * e), c1 = *(const f32x4*)(rp + 16 * e + 4), s0 = *(const f32x4*)(rp + 32 + 16 * e), s1 = *(const f32x4*)(rp + 32 + 16 * e + 4);
;           const v4u xa = *reinterpret_cast<v4u*>(&qr[8 + e]), xb = *reinterpret_cast<v4u*>(&qr[10 + e]); v4u ya, yb;
;     ...
;           ROPE2(x, c0[0], c0[1], s0[0], s0[1]); ROPE2(y, c0[2], c0[3], s0[2], s0[3]); ROPE2(z, c1[0], c1[1], s1[0], s1[1]); ROPE2(w, c1[2], c1[3], s1[2], s1[3]);
;     ...
;           qr[8 + e] = *reinterpret_cast<bf16x8*>(&ya); qr[10 + e] = *reinterpret_cast<bf16x8*>(&yb); } }
;     const int vb0 = (int)(uintptr_t)(lds) + v_rd_base(lane);
;     LAS float* wsf = (LAS float*)(lds + W_OFF) + wid * 64; LAS float* li_l = wsf; LAS float* al_l = wsf + 32;
;     unsigned so[5];
; #pragma unroll
;     for (int p = 0; p < 2; ++p) { const int s = p * 512 + tid;
;         { const int sub = s >> 5, within = s & 31, kk = (sub >> 2) * 8 + (within >> 2), k = (kk & ~0xC) | ((kk & 4) << 1) | ((kk & 8) >> 1), c = (sub & 3) * 32 + (within & 3) * 8;
;           so[p] = (unsigned)(k * 2048 + h * 256 + 128 + c); }
;         { const int row = s >> 4, chunk = (s & 15) ^ (row & 7); so[2 + p] = (unsigned)(row * 2048 + h * 256 + chunk * 8); } }
;     { const int row = tid >> 3, chunk = (tid & 7) ^ ((row >> 1) & 7); so[4] = (unsigned)(row * 64 + chunk * 8); }
;     const bf16* KVt = KV + tok0 * 2048; const bf16* KPt = KPE + tok0 * 64;
;     ...
;     float m_reg = -1e30f, l_reg = 0.f; f32x16 o[4] = {};
;     f32x16 p0, p1; float mn, alpha; bf16x8 pa0, pa1, pa2, pa3;
;     asm volatile("s_waitcnt vmcnt(0)" ::: "memory");
;     AISSUE(0, 0); AISSUE(1, BUFB);
	v_lshlrev_b32_e32 v27, 16, v0
	v_sub_f32_e32 v9, v13, v12
	v_mov_b32_e32 v12, v32
	v_mov_b32_e32 v13, v28
	v_pk_mul_f32 v[10:11], v[12:13], v[10:11]
	v_mov_b32_e32 v32, v29
	v_add_f32_e32 v14, v10, v11
	v_and_b32_e32 v11, 0xffff0000, v21
	v_and_b32_e32 v10, 0xffff0000, v25
	v_pk_mul_f32 v[12:13], v[32:33], v[10:11]
	v_mov_b32_e32 v28, v33
	v_sub_f32_e32 v12, v13, v12
	v_pk_mul_f32 v[10:11], v[28:29], v[10:11]
	v_cvt_pk_bf16_f32 v131, v9, v12
	s_waitcnt vmcnt(0)
	v_lshlrev_b32_e32 v26, 16, v4
	v_add_f32_e32 v9, v10, v11
	v_cvt_pk_bf16_f32 v135, v14, v9
	global_load_dwordx4 v[10:13], v[34:35], off offset:192
	global_load_dwordx4 v[14:17], v[34:35], off offset:64
	global_load_dwordx4 v[18:21], v[34:35], off offset:208
	global_load_dwordx4 v[22:25], v[34:35], off offset:80
	v_and_b32_e32 v29, 0xffff0000, v0
	v_and_b32_e32 v28, 0xffff0000, v4
	v_lshlrev_b32_e32 v31, 16, v1
	v_and_b32_e32 v1, 0xffff0000, v1
	v_lshlrev_b32_e32 v30, 16, v5
	s_waitcnt vmcnt(3)
	v_mov_b32_e32 v32, v10
	s_waitcnt vmcnt(2)
	v_mov_b32_e32 v33, v14
	v_mov_b32_e32 v34, v14
	v_mov_b32_e32 v35, v10
	v_mov_b32_e32 v14, v11
	v_pk_mul_f32 v[32:33], v[32:33], v[26:27]
	v_mov_b32_e32 v10, v15
	v_pk_mul_f32 v[26:27], v[34:35], v[26:27]
	v_pk_mul_f32 v[14:15], v[14:15], v[28:29]
	v_sub_f32_e32 v0, v33, v32
	v_mov_b32_e32 v36, v12
	v_mov_b32_e32 v37, v16
	v_mov_b32_e32 v38, v16
	v_pk_mul_f32 v[10:11], v[10:11], v[28:29]
	v_add_f32_e32 v4, v26, v27
	v_sub_f32_e32 v9, v15, v14
	v_cvt_pk_bf16_f32 v136, v0, v9
	v_mov_b32_e32 v39, v12
	v_and_b32_e32 v0, 0xffff0000, v5
	v_mov_b32_e32 v16, v13
	v_mov_b32_e32 v12, v17
	v_add_f32_e32 v10, v10, v11
	v_cvt_pk_bf16_f32 v140, v4, v10
	v_pk_mul_f32 v[4:5], v[16:17], v[0:1]
	v_pk_mul_f32 v[0:1], v[12:13], v[0:1]
	v_pk_mul_f32 v[28:29], v[36:37], v[30:31]
	v_pk_mul_f32 v[10:11], v[38:39], v[30:31]
	v_sub_f32_e32 v4, v5, v4
	v_add_f32_e32 v0, v0, v1
	v_sub_f32_e32 v14, v29, v28
	v_add_f32_e32 v9, v10, v11
	v_cvt_pk_bf16_f32 v137, v14, v4
	v_cvt_pk_bf16_f32 v141, v9, v0
	v_lshlrev_b32_e32 v1, 16, v2
	v_lshlrev_b32_e32 v0, 16, v6
	s_waitcnt vmcnt(1)
	v_mov_b32_e32 v4, v18
	s_waitcnt vmcnt(0)
	v_mov_b32_e32 v5, v22
	v_pk_mul_f32 v[4:5], v[4:5], v[0:1]
	v_mov_b32_e32 v14, v145
	v_sub_f32_e32 v9, v5, v4
	v_mov_b32_e32 v4, v22
	v_mov_b32_e32 v5, v18
	v_pk_mul_f32 v[0:1], v[4:5], v[0:1]
	v_mov_b32_e32 v22, v19
	v_add_f32_e32 v10, v0, v1
	v_and_b32_e32 v1, 0xffff0000, v2
	v_and_b32_e32 v0, 0xffff0000, v6
	v_mov_b32_e32 v18, v23
	v_pk_mul_f32 v[4:5], v[22:23], v[0:1]
	v_pk_mul_f32 v[0:1], v[18:19], v[0:1]
	v_sub_f32_e32 v2, v5, v4
	v_add_f32_e32 v0, v0, v1
	v_cvt_pk_bf16_f32 v138, v9, v2
	v_cvt_pk_bf16_f32 v142, v10, v0
	v_lshlrev_b32_e32 v1, 16, v3
	v_lshlrev_b32_e32 v0, 16, v7
	v_mov_b32_e32 v4, v20
	v_mov_b32_e32 v5, v24
	v_pk_mul_f32 v[4:5], v[4:5], v[0:1]
	v_lshlrev_b32_e32 v9, 3, v159
	v_sub_f32_e32 v6, v5, v4
	v_mov_b32_e32 v4, v24
	v_mov_b32_e32 v5, v20
	v_pk_mul_f32 v[0:1], v[4:5], v[0:1]
	v_mov_b32_e32 v24, v21
	v_add_f32_e32 v4, v0, v1
	v_and_b32_e32 v1, 0xffff0000, v3
	v_and_b32_e32 v0, 0xffff0000, v7
	v_mov_b32_e32 v20, v25
	v_pk_mul_f32 v[2:3], v[24:25], v[0:1]
	v_pk_mul_f32 v[0:1], v[20:21], v[0:1]
	v_sub_f32_e32 v2, v3, v2
	v_add_f32_e32 v0, v0, v1
	v_cvt_pk_bf16_f32 v139, v6, v2
	v_cvt_pk_bf16_f32 v143, v4, v0
	v_bfe_u32 v0, v159, 2, 2
	v_lshrrev_b32_e32 v1, 1, v159
	v_and_b32_e32 v3, 15, v159
	v_ashrrev_i32_e32 v4, 4, v159
	v_and_or_b32 v1, v1, 8, v0
	v_and_b32_e32 v0, 0x60, v159
	v_and_b32_e32 v2, 24, v9
	v_bitop3_b32 v7, v4, v3, 7 bitop3:0x6c
	v_or3_b32 v5, v0, v2, s92
	v_and_b32_e32 v0, 0x1ffff0, v4
	v_lshrrev_b32_e32 v6, 1, v4
	v_lshlrev_b32_e32 v4, 11, v4
	v_lshlrev_b32_e32 v7, 3, v7
	v_or3_b32 v146, v7, v4, s92
	v_add_u32_e32 v4, 0x200, v159
	v_and_b32_e32 v6, 4, v6
	v_ashrrev_i32_e32 v4, 4, v4
	v_or3_b32 v0, v0, v6, v1
	v_lshrrev_b32_e32 v10, 1, v4
	v_lshlrev_b32_e32 v6, 11, v0
	v_and_b32_e32 v7, 0x1ffff0, v4
	v_and_b32_e32 v10, 4, v10
	v_or_b32_e32 v2, 0x80, v5
	v_or3_b32 v1, v7, v10, v1
	v_or_b32_e32 v150, v6, v5
	v_or_b32_e32 v0, v6, v2
	v_lshlrev_b32_e32 v10, 11, v1
	v_lshl_add_u64 v[6:7], v[150:151], 1, s[96:97]
	s_waitcnt vmcnt(0)
	v_lshl_add_u64 v[6:7], v[6:7], 0, s[66:67]
	v_or_b32_e32 v152, v10, v5
	v_bitop3_b32 v1, v4, v3, 7 bitop3:0x6c
	global_load_lds_dwordx4 v[6:7], off
	v_lshl_add_u64 v[6:7], v[152:153], 1, s[96:97]
	v_lshlrev_b32_e32 v3, 11, v4
	v_lshlrev_b32_e32 v1, 3, v1
	v_lshl_add_u64 v[6:7], v[6:7], 0, s[66:67]
	s_add_i32 m0, s95, 0x2000
	v_or3_b32 v148, v1, v3, s92
	v_lshrrev_b32_e32 v1, 4, v159
	global_load_lds_dwordx4 v[6:7], off
	v_lshlrev_b64 v[6:7], 1, v[146:147]
	v_or_b32_e32 v2, v10, v2
	v_xor_b32_e32 v1, v1, v159
	v_lshl_add_u64 v[10:11], s[96:97], 0, v[6:7]
	s_add_i32 m0, s95, 0x4000
	v_and_b32_e32 v3, 0xffffffc0, v9
	v_lshlrev_b32_e32 v1, 3, v1
	global_load_lds_dwordx4 v[10:11], off
	v_lshlrev_b64 v[10:11], 1, v[148:149]
	v_and_or_b32 v4, v1, 56, v3
	v_lshl_add_u64 v[12:13], s[96:97], 0, v[10:11]
	s_add_i32 m0, s95, 0x6000
	v_mov_b32_e32 v5, v145
	global_load_lds_dwordx4 v[12:13], off
	v_lshl_add_u64 v[4:5], v[4:5], 1, s[0:1]
	s_mov_b64 s[0:1], 0xb928000
	s_add_i32 m0, s95, 0x8000
	v_lshl_add_u64 v[154:155], v[4:5], 0, s[0:1]
	s_add_u32 s0, s4, 0xd468000
	v_mov_b32_e32 v1, v145
	s_addc_u32 s1, s5, 0
	v_mov_b32_e32 v3, v145
	global_load_lds_dwordx4 v[154:155], off
	v_lshl_add_u64 v[0:1], v[0:1], 1, s[0:1]
	s_add_i32 m0, s95, 0xa000
	v_mov_b32_e32 v15, v145
	global_load_lds_dwordx4 v[0:1], off
	v_lshl_add_u64 v[0:1], v[2:3], 1, s[0:1]
	s_add_i32 m0, s95, 0xc000
	v_lshlrev_b32_e32 v2, 1, v159
	global_load_lds_dwordx4 v[0:1], off
	v_lshl_add_u64 v[0:1], s[0:1], 0, v[6:7]
	s_add_i32 m0, s95, 0xe000
; #define LAS __attribute__((address_space(3)))
; #define SBAR() __builtin_amdgcn_sched_barrier(0)
; __device__ __forceinline__ void qkt(f32x16& p0, f32x16& p1, LAS unsigned char* lds  , int r32, int hi, const bf16x8* qr) {
;     p0 = f32x16{}; p1 = f32x16{};
;     const LAS unsigned char* kb[4];
; #pragma unroll
;     for (int dd = 0; dd < 4; ++dd) kb[dd] = lds + K_OFF + KSWZ(r32, (dd * 16 + hi * 8) * 2);
; #pragma unroll
;     for (int d0 = 0; d0 < 8; ++d0) { const LAS unsigned char* a = kb[d0 & 3] + (d0 >> 2) * 128;
;         const bf16x8 b0 = *(const LAS bf16x8*)(a);
;         const bf16x8 b1 = *(const LAS bf16x8*)(a + 32 * 256);
;         p0 = __builtin_amdgcn_mfma_f32_32x32x16_bf16(b0, qr[d0], p0, 0, 0, 0);
;         p1 = __builtin_amdgcn_mfma_f32_32x32x16_bf16(b1, qr[d0], p1, 0, 0, 0); }
; #pragma unroll
;     for (int e = 0; e < 4; ++e) { const LAS unsigned char* a = lds + P_OFF + KPSWZ(r32, (e * 2 + hi) * 16);
;         const bf16x8 b0 = *(const LAS bf16x8*)(a);
;         const bf16x8 b1 = *(const LAS bf16x8*)(a + 32 * 128);
;         p0 = __builtin_amdgcn_mfma_f32_32x32x16_bf16(b0, qr[8 + e], p0, 0, 0, 0);
;         p1 = __builtin_amdgcn_mfma_f32_32x32x16_bf16(b1, qr[8 + e], p1, 0, 0, 0); }
; }
; __device__ __forceinline__ void attn_unit(LAS unsigned char* lds, int b, int h, int qb, const bf16* Q  , const bf16* KV  , const bf16* KPE  ,
;                                           const float* ROPE  , bf16* O  , const int wave_) {
;     ...
;     for (int t = 0; t < NT; ++t) {
;         asm volatile("s_waitcnt vmcnt(5)" ::: "memory"); __builtin_amdgcn_s_barrier();
;         { const int tn = (t + 2 < NT) ? t + 2 : NT - 1; AISSUE(tn, bl); }
;         const int kb_ = t * KVBLK;
;         if (kb_ <= qlo + 31) {
;             SBAR(); qkt(p0, p1, lds + bc, r32, hi, qr);
;             if (kb_ + KVBLK - 1 > qlo) mask_tile(p0, p1, qm - kb_);
	v_mov_b32_e32 v6, v145
	global_load_lds_dwordx4 v[0:1], off
	v_lshl_add_u64 v[0:1], s[0:1], 0, v[10:11]
	s_add_i32 m0, s95, 0x10000
	s_mov_b64 s[0:1], 0xb92a000
	global_load_lds_dwordx4 v[0:1], off
	v_lshl_add_u64 v[0:1], v[4:5], 0, s[0:1]
	s_add_i32 m0, s95, 0x12000
	s_movk_i32 s1, 0x70
	global_load_lds_dwordx4 v[0:1], off
	v_lshlrev_b32_e32 v1, 4, v159
	v_and_b32_e32 v0, 63, v159
	s_movk_i32 s0, 0x60
	v_and_b32_e32 v3, 0xc0, v1
	v_and_b32_e32 v4, 0x118, v9
	v_and_b32_e32 v5, 0x70, v1
	v_bitop3_b32 v161, v8, v1, s1 bitop3:0x78
	v_and_b32_e32 v1, 0x70, v9
	v_bitop3_b32 v165, v8, v5, s0 bitop3:0x36
	v_bitop3_b32 v167, v8, v9, s1 bitop3:0x78
	v_bitop3_b32 v170, v8, v1, s0 bitop3:0x36
	v_cmp_gt_u32_e64 s[0:1], 32, v0
	v_and_or_b32 v0, v2, 32, v4
	v_add3_u32 v171, v3, 0, v0
	v_or_b32_e32 v0, s33, v144
	v_bitop3_b32 v162, v8, v5, 32 bitop3:0x36
	v_bitop3_b32 v163, v8, v5, 64 bitop3:0x36
	v_bitop3_b32 v168, v8, v1, 32 bitop3:0x36
	v_bitop3_b32 v169, v8, v1, 64 bitop3:0x36
	v_sub_u32_e32 v172, v0, v156
	v_mov_b32_e32 v0, v145
	v_mov_b32_e32 v1, v145
	v_mov_b32_e32 v2, v145
	v_mov_b32_e32 v3, v145
	v_mov_b32_e32 v4, v145
	v_mov_b32_e32 v5, v145
	v_mov_b32_e32 v7, v145
	v_mov_b32_e32 v8, v145
	v_mov_b32_e32 v9, v145
	v_mov_b32_e32 v10, v145
	v_mov_b32_e32 v11, v145
	v_mov_b32_e32 v12, v145
	v_mov_b32_e32 v13, v145
	v_mov_b64_e32 v[30:31], v[14:15]
	v_mov_b64_e32 v[46:47], v[14:15]
	v_mov_b64_e32 v[62:63], v[14:15]
	s_add_i32 s2, s3, -1
	s_or_b32 s68, s33, 31
	v_mov_b64_e32 v[28:29], v[12:13]
	v_mov_b64_e32 v[26:27], v[10:11]
	v_mov_b64_e32 v[24:25], v[8:9]
	v_mov_b64_e32 v[22:23], v[6:7]
	v_mov_b64_e32 v[20:21], v[4:5]
	v_mov_b64_e32 v[18:19], v[2:3]
	v_mov_b64_e32 v[16:17], v[0:1]
	v_mov_b64_e32 v[44:45], v[12:13]
	v_mov_b64_e32 v[42:43], v[10:11]
	v_mov_b64_e32 v[40:41], v[8:9]
	v_mov_b64_e32 v[38:39], v[6:7]
	v_mov_b64_e32 v[36:37], v[4:5]
	v_mov_b64_e32 v[34:35], v[2:3]
	v_mov_b64_e32 v[32:33], v[0:1]
	v_mov_b64_e32 v[60:61], v[12:13]
	v_mov_b64_e32 v[58:59], v[10:11]
	v_mov_b64_e32 v[56:57], v[8:9]
	v_mov_b64_e32 v[54:55], v[6:7]
	v_mov_b64_e32 v[52:53], v[4:5]
	v_mov_b64_e32 v[50:51], v[2:3]
	v_mov_b64_e32 v[48:49], v[0:1]
	s_cmp_lt_u32 s89, 4
	s_cbranch_scc1 .Lattn_lo
	s_setprio 1
.Lattn_lo:
.LBB0_720:
	s_add_i32 s4, s73, 2
	s_min_u32 s70, s4, s2
	s_lshl_b64 s[4:5], s[70:71], 18
	s_add_u32 s4, s96, s4
	s_addc_u32 s5, s97, s5
	v_lshl_add_u64 v[64:65], v[150:151], 1, s[4:5]
	s_add_i32 s8, s95, s69
	v_lshl_add_u64 v[64:65], v[64:65], 0, s[66:67]
	s_mov_b32 m0, s8
	s_waitcnt vmcnt(5)
	s_barrier
	global_load_lds_dwordx4 v[64:65], off
	v_lshl_add_u64 v[64:65], v[152:153], 1, s[4:5]
	v_lshl_add_u64 v[64:65], v[64:65], 0, s[66:67]
	s_add_i32 m0, s8, 0x2000
	s_lshl_b64 s[6:7], s[70:71], 13
	global_load_lds_dwordx4 v[64:65], off
	v_lshl_add_u64 v[64:65], v[146:147], 1, s[4:5]
	s_add_i32 m0, s8, 0x4000
	s_nop 0
	global_load_lds_dwordx4 v[64:65], off
	v_lshl_add_u64 v[64:65], v[148:149], 1, s[4:5]
	s_add_i32 m0, s8, 0x6000
	s_sub_i32 s4, s94, 63
	global_load_lds_dwordx4 v[64:65], off
	v_lshl_add_u64 v[64:65], v[154:155], 0, s[6:7]
	s_add_i32 m0, s8, 0x8000
	s_cmp_gt_i32 s4, s68
	global_load_lds_dwordx4 v[64:65], off
	s_cbranch_scc1 .LBB0_728
	s_add_i32 s4, s72, 0
	v_add_u32_e32 v216, s4, v160
	v_add_u32_e32 v220, s4, v166
	v_add_u32_e32 v217, v216, v162
	v_add_u32_e32 v218, v216, v163
	v_add_u32_e32 v219, v216, v165
	v_add_u32_e32 v216, v216, v161
	v_add_u32_e32 v221, v220, v168
	v_add_u32_e32 v222, v220, v169
	v_add_u32_e32 v223, v220, v170
	v_add_u32_e32 v220, v220, v167
	ds_read_b128 v[176:179], v216 offset:16384
	ds_read_b128 v[180:183], v216 offset:24576
	ds_read_b128 v[184:187], v217 offset:16384
	ds_read_b128 v[188:191], v217 offset:24576
	ds_read_b128 v[192:195], v218 offset:16384
	ds_read_b128 v[196:199], v218 offset:24576
	ds_read_b128 v[200:203], v219 offset:16384
	ds_read_b128 v[204:207], v219 offset:24576
	s_cmp_le_i32 s94, s33
	ds_read_b128 v[208:211], v216 offset:16512
	ds_read_b128 v[212:215], v216 offset:24704
	s_waitcnt lgkmcnt(8)
	v_mfma_f32_32x32x16_bf16 v[80:95], v[176:179], v[124:127], 0
	v_mfma_f32_32x32x16_bf16 v[64:79], v[180:183], v[124:127], 0
	ds_read_b128 v[176:179], v217 offset:16512
	ds_read_b128 v[180:183], v217 offset:24704
	s_waitcnt lgkmcnt(8)
	v_mfma_f32_32x32x16_bf16 v[80:95], v[184:187], v[100:103], v[80:95]
	v_mfma_f32_32x32x16_bf16 v[64:79], v[188:191], v[100:103], v[64:79]
	ds_read_b128 v[184:187], v218 offset:16512
	ds_read_b128 v[188:191], v218 offset:24704
	s_waitcnt lgkmcnt(8)
	v_mfma_f32_32x32x16_bf16 v[80:95], v[192:195], v[104:107], v[80:95]
	v_mfma_f32_32x32x16_bf16 v[64:79], v[196:199], v[104:107], v[64:79]
	ds_read_b128 v[192:195], v219 offset:16512
	ds_read_b128 v[196:199], v219 offset:24704
	s_waitcnt lgkmcnt(8)
	v_mfma_f32_32x32x16_bf16 v[80:95], v[200:203], v[108:111], v[80:95]
	v_mfma_f32_32x32x16_bf16 v[64:79], v[204:207], v[108:111], v[64:79]
	ds_read_b128 v[200:203], v220 offset:32768
	ds_read_b128 v[204:207], v220 offset:36864
	s_waitcnt lgkmcnt(8)
	v_mfma_f32_32x32x16_bf16 v[80:95], v[208:211], v[112:115], v[80:95]
	v_mfma_f32_32x32x16_bf16 v[64:79], v[212:215], v[112:115], v[64:79]
	ds_read_b128 v[208:211], v221 offset:32768
	ds_read_b128 v[212:215], v221 offset:36864
	s_waitcnt lgkmcnt(8)
	v_mfma_f32_32x32x16_bf16 v[80:95], v[176:179], v[116:119], v[80:95]
	v_mfma_f32_32x32x16_bf16 v[64:79], v[180:183], v[116:119], v[64:79]
	ds_read_b128 v[176:179], v222 offset:32768
	ds_read_b128 v[180:183], v222 offset:36864
	s_waitcnt lgkmcnt(8)
	v_mfma_f32_32x32x16_bf16 v[80:95], v[184:187], v[120:123], v[80:95]
	v_mfma_f32_32x32x16_bf16 v[64:79], v[188:191], v[120:123], v[64:79]
	ds_read_b128 v[184:187], v223 offset:32768
	ds_read_b128 v[188:191], v223 offset:36864
	s_waitcnt lgkmcnt(8)
	v_mfma_f32_32x32x16_bf16 v[80:95], v[192:195], v[96:99], v[80:95]
	v_mfma_f32_32x32x16_bf16 v[64:79], v[196:199], v[96:99], v[64:79]
	s_waitcnt lgkmcnt(6)
	v_mfma_f32_32x32x16_bf16 v[80:95], v[200:203], v[128:131], v[80:95]
	v_mfma_f32_32x32x16_bf16 v[64:79], v[204:207], v[128:131], v[64:79]
	s_waitcnt lgkmcnt(4)
	v_mfma_f32_32x32x16_bf16 v[80:95], v[208:211], v[136:139], v[80:95]
	v_mfma_f32_32x32x16_bf16 v[64:79], v[212:215], v[136:139], v[64:79]
	s_waitcnt lgkmcnt(2)
	v_mfma_f32_32x32x16_bf16 v[80:95], v[176:179], v[132:135], v[80:95]
	v_mfma_f32_32x32x16_bf16 v[64:79], v[180:183], v[132:135], v[64:79]
	s_waitcnt lgkmcnt(0)
	v_mfma_f32_32x32x16_bf16 v[80:95], v[184:187], v[140:143], v[80:95]
	v_mfma_f32_32x32x16_bf16 v[64:79], v[188:191], v[140:143], v[64:79]
	v_add_u32_e32 v252, s72, v171
	ds_read_b64_tr_b16 v[224:225], v252 offset:0
	ds_read_b64_tr_b16 v[226:227], v252 offset:2048
	ds_read_b64_tr_b16 v[228:229], v252 offset:4096
	ds_read_b64_tr_b16 v[230:231], v252 offset:6144
	ds_read_b64_tr_b16 v[232:233], v252 offset:8192
	ds_read_b64_tr_b16 v[234:235], v252 offset:10240
	ds_read_b64_tr_b16 v[236:237], v252 offset:12288
	ds_read_b64_tr_b16 v[238:239], v252 offset:14336
	s_cbranch_scc1 .LBB0_723
; __device__ __forceinline__ void mask_tile(f32x16& p0, f32x16& p1, int dq) {
;     const float NEG = -__builtin_inff();
; #pragma unroll
;     for (int r = 0; r < 16; ++r) { const int c = (r & 3) + 8 * (r >> 2);
;         if (dq - c < 0) p0[r] = NEG;
;         if (dq - c - 32 < 0) p1[r] = NEG; }
; }
; __device__ __forceinline__ void attn_unit(LAS unsigned char* lds, int b, int h, int qb, const bf16* Q  , const bf16* KV  , const bf16* KPE  ,
;                                           const float* ROPE  , bf16* O  , const int wave_) {
;     ...
;             if (kb_ + KVBLK - 1 > qlo) mask_tile(p0, p1, qm - kb_);
	v_cmp_gt_i32_e64 s[62:63], 26, v172
	v_cmp_gt_i32_e64 s[64:65], 27, v172
	v_cmp_gt_i32_e64 s[60:61], 25, v172
	s_and_b64 s[62:63], s[64:65], s[62:63]
	v_cmp_gt_i32_e64 s[58:59], 24, v172
	s_and_b64 s[60:61], s[62:63], s[60:61]
	v_cmp_gt_i32_e64 s[56:57], 19, v172
	s_and_b64 s[58:59], s[60:61], s[58:59]
	v_cmp_gt_i32_e64 s[54:55], 18, v172
	s_and_b64 s[56:57], s[58:59], s[56:57]
	v_cmp_gt_i32_e64 s[52:53], 17, v172
	s_and_b64 s[54:55], s[56:57], s[54:55]
	v_cmp_gt_i32_e64 s[50:51], 16, v172
	s_and_b64 s[52:53], s[54:55], s[52:53]
	v_cmp_gt_i32_e64 s[48:49], 11, v172
	s_and_b64 s[50:51], s[52:53], s[50:51]
	v_cmp_gt_i32_e64 s[46:47], 10, v172
	s_and_b64 s[48:49], s[50:51], s[48:49]
	v_cmp_gt_i32_e64 s[44:45], 9, v172
	s_and_b64 s[46:47], s[48:49], s[46:47]
	v_cmp_gt_i32_e64 s[42:43], 8, v172
	s_and_b64 s[44:45], s[46:47], s[44:45]
	v_cmp_gt_i32_e64 s[40:41], 3, v172
	s_and_b64 s[42:43], s[44:45], s[42:43]
	v_cmp_gt_i32_e64 s[38:39], 2, v172
	s_and_b64 s[40:41], s[42:43], s[40:41]
	v_cmp_gt_i32_e64 s[36:37], 1, v172
	s_and_b64 s[38:39], s[40:41], s[38:39]
	v_cmp_gt_i32_e64 s[34:35], 0, v172
	s_and_b64 s[36:37], s[38:39], s[36:37]
	s_and_b64 s[34:35], s[36:37], s[34:35]
	v_cmp_gt_i32_e64 s[30:31], 58, v172
	v_cndmask_b32_e64 v80, v80, v173, s[34:35]
	v_cmp_gt_i32_e64 s[34:35], 59, v172
	v_cmp_gt_i32_e64 s[28:29], 57, v172
	s_and_b64 s[30:31], s[34:35], s[30:31]
	v_cmp_gt_i32_e64 s[26:27], 56, v172
	s_and_b64 s[28:29], s[30:31], s[28:29]
	v_cmp_gt_i32_e64 s[24:25], 51, v172
	s_and_b64 s[26:27], s[28:29], s[26:27]
	v_cmp_gt_i32_e64 s[22:23], 50, v172
	s_and_b64 s[24:25], s[26:27], s[24:25]
	v_cmp_gt_i32_e64 s[20:21], 49, v172
	s_and_b64 s[22:23], s[24:25], s[22:23]
	v_cmp_gt_i32_e64 s[18:19], 48, v172
	s_and_b64 s[20:21], s[22:23], s[20:21]
	v_cmp_gt_i32_e64 s[16:17], 43, v172
	s_and_b64 s[18:19], s[20:21], s[18:19]
	v_cmp_gt_i32_e64 s[14:15], 42, v172
	s_and_b64 s[16:17], s[18:19], s[16:17]
	v_cmp_gt_i32_e64 s[12:13], 41, v172
	s_and_b64 s[14:15], s[16:17], s[14:15]
	v_cmp_gt_i32_e64 s[10:11], 40, v172
	s_and_b64 s[12:13], s[14:15], s[12:13]
	v_cmp_gt_i32_e64 s[8:9], 35, v172
	s_and_b64 s[10:11], s[12:13], s[10:11]
	v_cmp_gt_i32_e64 s[6:7], 34, v172
	s_and_b64 s[8:9], s[10:11], s[8:9]
	v_cmp_gt_i32_e64 s[4:5], 33, v172
	v_cndmask_b32_e64 v94, v94, v173, s[62:63]
	v_cndmask_b32_e64 v93, v93, v173, s[60:61]
	v_cndmask_b32_e64 v92, v92, v173, s[58:59]
	v_cndmask_b32_e64 v91, v91, v173, s[56:57]
	v_cndmask_b32_e64 v90, v90, v173, s[54:55]
	v_cndmask_b32_e64 v89, v89, v173, s[52:53]
	v_cndmask_b32_e64 v88, v88, v173, s[50:51]
	v_cndmask_b32_e64 v87, v87, v173, s[48:49]
	v_readlane_b32 s48, v254, 42
	s_and_b64 s[6:7], s[8:9], s[6:7]
	v_cmp_gt_i32_e32 vcc, 32, v172
	v_readlane_b32 s52, v254, 46
	v_readlane_b32 s53, v254, 47
	v_readlane_b32 s56, v254, 50
	v_readlane_b32 s57, v254, 51
	v_readlane_b32 s58, v254, 52
	v_readlane_b32 s59, v254, 53
	v_readlane_b32 s60, v254, 54
	v_readlane_b32 s61, v254, 55
	s_and_b64 s[4:5], s[6:7], s[4:5]
	v_readlane_b32 s62, v254, 56
	v_readlane_b32 s63, v254, 57
	s_mov_b64 s[52:53], s[56:57]
	s_mov_b64 s[56:57], s[60:61]
	s_and_b64 vcc, s[4:5], vcc
	v_cndmask_b32_e64 v95, v95, v173, s[64:65]
	s_mov_b64 s[58:59], s[62:63]
	v_cndmask_b32_e64 v86, v86, v173, s[46:47]
	v_cndmask_b32_e64 v85, v85, v173, s[44:45]
	v_cndmask_b32_e64 v84, v84, v173, s[42:43]
	v_cndmask_b32_e64 v83, v83, v173, s[40:41]
	v_cndmask_b32_e64 v82, v82, v173, s[38:39]
	v_cndmask_b32_e64 v81, v81, v173, s[36:37]
	v_cndmask_b32_e64 v79, v79, v173, s[34:35]
	v_cndmask_b32_e64 v78, v78, v173, s[30:31]
	v_cndmask_b32_e64 v77, v77, v173, s[28:29]
	v_cndmask_b32_e64 v76, v76, v173, s[26:27]
	v_cndmask_b32_e64 v75, v75, v173, s[24:25]
	v_cndmask_b32_e64 v74, v74, v173, s[22:23]
	v_cndmask_b32_e64 v73, v73, v173, s[20:21]
	v_cndmask_b32_e64 v72, v72, v173, s[18:19]
	v_cndmask_b32_e64 v71, v71, v173, s[16:17]
	v_cndmask_b32_e64 v70, v70, v173, s[14:15]
	v_cndmask_b32_e64 v69, v69, v173, s[12:13]
	v_cndmask_b32_e64 v68, v68, v173, s[10:11]
	v_cndmask_b32_e64 v67, v67, v173, s[8:9]
	v_cndmask_b32_e64 v66, v66, v173, s[6:7]
	v_cndmask_b32_e64 v65, v65, v173, s[4:5]
	v_cndmask_b32_e32 v64, v64, v173, vcc
	v_readlane_b32 s49, v254, 43
	v_readlane_b32 s50, v254, 44
	v_readlane_b32 s51, v254, 45
	v_readlane_b32 s54, v254, 48
	v_readlane_b32 s55, v254, 49

; #define LDS_WAIT() asm volatile("s_waitcnt lgkmcnt(0)" ::: "memory")
; __device__ __forceinline__ int crow(int r, int hi) { return (r & 3) + 8 * (r >> 2) + 4 * hi; }
; __device__ __forceinline__ unsigned cvtpk(float lo, float hi) { unsigned r; asm volatile("v_cvt_pk_bf16_f32 %0, %1, %2" : "=v"(r) : "v"(lo), "v"(hi)); return r; }
; __device__ __forceinline__ void attn_unit(LAS unsigned char* lds, int b, int h, int qb, const bf16* Q  , const bf16* KV  , const bf16* KPE  ,
;                                           const float* ROPE  , bf16* O  , const int wave_) {
;     ...
;     asm volatile("s_waitcnt vmcnt(0)" ::: "memory");
;     if (hi == 0) li_l[r32] = l_reg; LDS_WAIT();
;     bf16* Ow = O + (tok0 + qlo) * 1024 + h * 128;
; #pragma unroll
;     for (int r = 0; r < 16; ++r) { const int orow = crow(r, hi); const float rl = __builtin_amdgcn_rcpf(li_l[orow]);
; #pragma unroll
;         for (int d0 = 0; d0 < 4; ++d0) { const float v = o[d0][r] * rl; const float vn = __shfl_xor(v, 1);
;             if ((r32 & 1) == 0) *(unsigned*)(Ow + (size_t)orow * 1024 + d0 * 32 + r32) = cvtpk(v, vn); } }
.LBB0_731:
	s_setprio 0
	s_waitcnt vmcnt(0)
	s_and_saveexec_b64 s[4:5], s[0:1]
	ds_write_b32 v164, v145
	s_or_b64 exec, exec, s[4:5]
	s_waitcnt lgkmcnt(0)
	ds_read_b32 v67, v157
	v_mbcnt_lo_u32_b32 v64, -1, 0
	v_mbcnt_hi_u32_b32 v64, -1, v64
	v_and_b32_e32 v66, 64, v64
	v_xor_b32_e32 v65, 1, v64
	s_waitcnt lgkmcnt(0)
	v_rcp_f32_e32 v69, v67
	v_add_u32_e32 v66, 64, v66
	s_lshl_b64 s[0:1], s[86:87], 11
	v_cmp_lt_i32_e32 vcc, v65, v66
	s_add_u32 s0, s78, s0
	s_addc_u32 s1, s79, s1
	v_cndmask_b32_e32 v64, v64, v65, vcc
	v_lshlrev_b32_e32 v68, 2, v64
	v_mul_f32_e32 v48, v48, v69
	s_add_u32 s0, s0, s92
	ds_bpermute_b32 v70, v68, v48
	s_addc_u32 s1, s1, 0
	v_and_b32_e32 v64, 1, v159
	v_lshlrev_b32_e32 v66, 1, v144
	v_mov_b32_e32 v67, 0
	v_cmp_eq_u32_e32 vcc, 0, v64
	v_lshl_add_u64 v[64:65], s[0:1], 0, v[66:67]
	s_mov_b64 s[0:1], 0x10c28000
	v_lshl_add_u64 v[64:65], v[64:65], 0, s[0:1]
	v_lshlrev_b32_e32 v66, 13, v158
	v_lshl_add_u64 v[66:67], v[64:65], 0, v[66:67]
	s_and_saveexec_b64 s[0:1], vcc
	s_mov_b32 s96, s84
	s_mov_b32 s97, s85
	s_mov_b64 s[84:85], s[90:91]
	v_readlane_b32 s90, v254, 61
	s_mov_b32 s92, s74
	s_mov_b32 s94, s88
	v_readlane_b32 s91, v254, 62
	s_mov_b32 s87, s89
	s_mov_b32 s88, s75
	v_readlane_b32 s89, v254, 60
	s_cbranch_execz .LBB0_735
	s_waitcnt lgkmcnt(0)
	v_cvt_pk_bf16_f32 v48, v48, v70
	global_store_dword v[66:67], v48, off
